# fp8 GEMMs: unit-scale v_mfma_scale_f32_16x16x128_f8f6f4 replaced by the unscaled v_mfma_f32_16x16x128_f8f6f4 (same e4m3 operands, no v_mfma_ld_scale_b32)
# baseline (speedup 1.0000x reference)
; __device__ __forceinline__ void mfma_fp8(f32x4& c, v8i_t a, v8i_t b, int sc) { asm volatile("v_mfma_scale_f32_16x16x128_f8f6f4 %0, %1, %2, %0, %3, %3 op_sel_hi:[0,0,0]" : "+v"(c) : "v"(a), "v"(b), "v"(sc)); }
.LBB0_734:
	ds_read_b64_tr_b16 v[26:27], v224 offset:0
	ds_read_b64_tr_b16 v[28:29], v224 offset:1024
	ds_read_b64_tr_b16 v[30:31], v224 offset:8192
	ds_read_b64_tr_b16 v[32:33], v224 offset:9216
	ds_read_b64_tr_b16 v[18:19], v228 offset:0
	ds_read_b64_tr_b16 v[20:21], v228 offset:1024
	ds_read_b64_tr_b16 v[22:23], v228 offset:8192
	ds_read_b64_tr_b16 v[24:25], v228 offset:9216
	ds_read_b64_tr_b16 v[10:11], v225 offset:0
	ds_read_b64_tr_b16 v[12:13], v225 offset:1024
	ds_read_b64_tr_b16 v[14:15], v225 offset:8192
	ds_read_b64_tr_b16 v[16:17], v225 offset:9216
	ds_read_b64_tr_b16 v[2:3], v229 offset:0
	ds_read_b64_tr_b16 v[4:5], v229 offset:1024
	s_add_u32 s4, s38, 0xfffc0080
	ds_read_b64_tr_b16 v[6:7], v229 offset:8192
	s_addc_u32 s5, s39, -1
	ds_read_b64_tr_b16 v[8:9], v229 offset:9216
	s_cmp_eq_u32 s64, 12
	s_cselect_b32 s43, s19, s5
	s_cselect_b32 s42, s21, s4
	s_cselect_b32 s41, s29, s63
	s_cselect_b32 s40, s61, s62
	v_lshl_add_u64 v[68:69], s[38:39], 0, v[198:199]
	s_add_i32 m0, s15, 0xc000
	s_waitcnt lgkmcnt(0)
	ds_read_b128 v[34:37], v234
	ds_read_b128 v[38:41], v234 offset:1024
	ds_read_b128 v[42:45], v234 offset:2048
	ds_read_b128 v[46:49], v234 offset:3072
	ds_read_b128 v[50:53], v234 offset:4096
	ds_read_b128 v[54:57], v234 offset:5120
	ds_read_b128 v[58:61], v234 offset:6144
	ds_read_b128 v[62:65], v234 offset:7168
	global_load_lds_dwordx4 v[68:69], off
	v_lshl_add_u64 v[68:69], s[38:39], 0, v[200:201]
	s_add_i32 m0, s15, 0xe000
	s_nop 0
	global_load_lds_dwordx4 v[68:69], off
	s_waitcnt vmcnt(8)
	s_waitcnt lgkmcnt(0)
	s_barrier
	s_setprio 1
	s_waitcnt lgkmcnt(0)
	v_mfma_f32_16x16x128_f8f6f4 v[194:197], v[26:33], v[34:41], v[194:197]
	v_mfma_f32_16x16x128_f8f6f4 v[190:193], v[18:25], v[34:41], v[190:193]
	v_mfma_f32_16x16x128_f8f6f4 v[178:181], v[26:33], v[42:49], v[178:181]
	v_mfma_f32_16x16x128_f8f6f4 v[174:177], v[18:25], v[42:49], v[174:177]
	v_mfma_f32_16x16x128_f8f6f4 v[162:165], v[26:33], v[50:57], v[162:165]
	v_mfma_f32_16x16x128_f8f6f4 v[158:161], v[18:25], v[50:57], v[158:161]
	v_mfma_f32_16x16x128_f8f6f4 v[146:149], v[26:33], v[58:65], v[146:149]
	v_mfma_f32_16x16x128_f8f6f4 v[142:145], v[18:25], v[58:65], v[142:145]
	s_setprio 0
	s_setprio 1
	v_mfma_f32_16x16x128_f8f6f4 v[186:189], v[10:17], v[34:41], v[186:189]
	v_mfma_f32_16x16x128_f8f6f4 v[182:185], v[2:9], v[34:41], v[182:185]
	v_mfma_f32_16x16x128_f8f6f4 v[170:173], v[10:17], v[42:49], v[170:173]
	v_mfma_f32_16x16x128_f8f6f4 v[166:169], v[2:9], v[42:49], v[166:169]
	v_mfma_f32_16x16x128_f8f6f4 v[154:157], v[10:17], v[50:57], v[154:157]
	v_mfma_f32_16x16x128_f8f6f4 v[150:153], v[2:9], v[50:57], v[150:153]
	v_mfma_f32_16x16x128_f8f6f4 v[138:141], v[10:17], v[58:65], v[138:141]
	v_mfma_f32_16x16x128_f8f6f4 v[134:137], v[2:9], v[58:65], v[134:137]
	s_setprio 0
	s_barrier
	s_mov_b32 m0, s31
	v_lshl_add_u64 v[68:69], s[40:41], 0, v[214:215]
	s_add_u32 s4, s40, 0x1000
	ds_read_b128 v[58:61], v234 offset:16384
	ds_read_b128 v[62:65], v234 offset:17408
	ds_read_b128 v[50:53], v234 offset:18432
	ds_read_b128 v[54:57], v234 offset:19456
	ds_read_b128 v[42:45], v234 offset:20480
	ds_read_b128 v[46:49], v234 offset:21504
	ds_read_b128 v[34:37], v234 offset:22528
	ds_read_b128 v[38:41], v234 offset:23552
	global_load_lds_dwordx4 v[68:69], off
	v_lshl_add_u64 v[68:69], s[40:41], 0, v[218:219]
	s_mov_b32 m0, s33
	s_addc_u32 s5, s41, 0
	global_load_lds_dwordx4 v[68:69], off
	v_lshl_add_u64 v[68:69], s[4:5], 0, v[214:215]
	s_mov_b32 m0, s35
	v_lshl_add_u64 v[202:203], s[42:43], 0, v[216:217]
	global_load_lds_dwordx4 v[68:69], off
	v_lshl_add_u64 v[68:69], s[4:5], 0, v[218:219]
	s_mov_b32 m0, s46
	v_cmp_ne_u32_e64 s[4:5], 1, v237
	global_load_lds_dwordx4 v[68:69], off
	v_lshl_add_u64 v[68:69], s[42:43], 0, v[212:213]
	s_mov_b32 m0, s15
	s_andn2_b64 vcc, exec, s[36:37]
	global_load_lds_dwordx4 v[68:69], off
	s_mov_b32 m0, s47
	s_nop 0
	global_load_lds_dwordx4 v[202:203], off
	s_waitcnt vmcnt(8)
	s_waitcnt lgkmcnt(0)
	s_barrier
	s_cbranch_vccnz .LBB0_736
	s_setprio 1
	s_waitcnt lgkmcnt(0)
	v_mfma_f32_16x16x128_f8f6f4 v[130:133], v[26:33], v[58:65], v[130:133]
	v_mfma_f32_16x16x128_f8f6f4 v[126:129], v[18:25], v[58:65], v[126:129]
	v_mfma_f32_16x16x128_f8f6f4 v[114:117], v[26:33], v[50:57], v[114:117]
	v_mfma_f32_16x16x128_f8f6f4 v[110:113], v[18:25], v[50:57], v[110:113]
	v_mfma_f32_16x16x128_f8f6f4 v[98:101], v[26:33], v[42:49], v[98:101]
	v_mfma_f32_16x16x128_f8f6f4 v[94:97], v[18:25], v[42:49], v[94:97]
	v_mfma_f32_16x16x128_f8f6f4 v[82:85], v[26:33], v[34:41], v[82:85]
	v_mfma_f32_16x16x128_f8f6f4 v[78:81], v[18:25], v[34:41], v[78:81]
	s_setprio 0
	s_setprio 1
	v_mfma_f32_16x16x128_f8f6f4 v[122:125], v[10:17], v[58:65], v[122:125]
	v_mfma_f32_16x16x128_f8f6f4 v[118:121], v[2:9], v[58:65], v[118:121]
	v_mfma_f32_16x16x128_f8f6f4 v[106:109], v[10:17], v[50:57], v[106:109]
	v_mfma_f32_16x16x128_f8f6f4 v[102:105], v[2:9], v[50:57], v[102:105]
	v_mfma_f32_16x16x128_f8f6f4 v[90:93], v[10:17], v[42:49], v[90:93]
	v_mfma_f32_16x16x128_f8f6f4 v[86:89], v[2:9], v[42:49], v[86:89]
	v_mfma_f32_16x16x128_f8f6f4 v[74:77], v[10:17], v[34:41], v[74:77]
	v_mfma_f32_16x16x128_f8f6f4 v[70:73], v[2:9], v[34:41], v[70:73]
	s_setprio 0
.LBB0_736:
	s_add_u32 s44, s40, 0x84000
	s_addc_u32 s45, s41, 0
	s_barrier
	ds_read_b64_tr_b16 v[26:27], v226 offset:0
	ds_read_b64_tr_b16 v[28:29], v226 offset:1024
	ds_read_b64_tr_b16 v[30:31], v226 offset:8192
	ds_read_b64_tr_b16 v[32:33], v226 offset:9216
	ds_read_b64_tr_b16 v[18:19], v230 offset:0
	ds_read_b64_tr_b16 v[20:21], v230 offset:1024
	ds_read_b64_tr_b16 v[22:23], v230 offset:8192
	ds_read_b64_tr_b16 v[24:25], v230 offset:9216
	ds_read_b64_tr_b16 v[10:11], v227 offset:0
	ds_read_b64_tr_b16 v[12:13], v227 offset:1024
	ds_read_b64_tr_b16 v[14:15], v227 offset:8192
	ds_read_b64_tr_b16 v[16:17], v227 offset:9216
	ds_read_b64_tr_b16 v[2:3], v231 offset:0
	ds_read_b64_tr_b16 v[4:5], v231 offset:1024
	ds_read_b64_tr_b16 v[6:7], v231 offset:8192
	ds_read_b64_tr_b16 v[8:9], v231 offset:9216
	s_add_u32 s42, s42, 0x40000
	s_addc_u32 s43, s43, 0
	s_mov_b32 m0, s48
	v_lshl_add_u64 v[238:239], s[42:43], 0, v[212:213]
	s_waitcnt lgkmcnt(0)
	ds_read_b128 v[34:37], v234 offset:32768
	ds_read_b128 v[38:41], v234 offset:33792
	ds_read_b128 v[42:45], v234 offset:34816
	ds_read_b128 v[46:49], v234 offset:35840
	ds_read_b128 v[50:53], v234 offset:36864
	ds_read_b128 v[54:57], v234 offset:37888
	ds_read_b128 v[58:61], v234 offset:38912
	ds_read_b128 v[62:65], v234 offset:39936
	global_load_lds_dwordx4 v[238:239], off
	v_lshl_add_u64 v[238:239], s[42:43], 0, v[216:217]
	s_mov_b32 m0, s49
	s_nop 0
	global_load_lds_dwordx4 v[238:239], off
	s_waitcnt vmcnt(8)
	s_waitcnt lgkmcnt(0)
	s_barrier
	s_setprio 1
	s_waitcnt lgkmcnt(0)
	v_mfma_f32_16x16x128_f8f6f4 v[194:197], v[26:33], v[34:41], v[194:197]
	v_mfma_f32_16x16x128_f8f6f4 v[190:193], v[18:25], v[34:41], v[190:193]
	v_mfma_f32_16x16x128_f8f6f4 v[178:181], v[26:33], v[42:49], v[178:181]
	v_mfma_f32_16x16x128_f8f6f4 v[174:177], v[18:25], v[42:49], v[174:177]
	v_mfma_f32_16x16x128_f8f6f4 v[162:165], v[26:33], v[50:57], v[162:165]
	v_mfma_f32_16x16x128_f8f6f4 v[158:161], v[18:25], v[50:57], v[158:161]
	v_mfma_f32_16x16x128_f8f6f4 v[146:149], v[26:33], v[58:65], v[146:149]
	v_mfma_f32_16x16x128_f8f6f4 v[142:145], v[18:25], v[58:65], v[142:145]
	s_setprio 0
	s_setprio 1
	v_mfma_f32_16x16x128_f8f6f4 v[186:189], v[10:17], v[34:41], v[186:189]
	v_mfma_f32_16x16x128_f8f6f4 v[182:185], v[2:9], v[34:41], v[182:185]
	v_mfma_f32_16x16x128_f8f6f4 v[170:173], v[10:17], v[42:49], v[170:173]
	v_mfma_f32_16x16x128_f8f6f4 v[166:169], v[2:9], v[42:49], v[166:169]
	v_mfma_f32_16x16x128_f8f6f4 v[154:157], v[10:17], v[50:57], v[154:157]
	v_mfma_f32_16x16x128_f8f6f4 v[150:153], v[2:9], v[50:57], v[150:153]
	v_mfma_f32_16x16x128_f8f6f4 v[138:141], v[10:17], v[58:65], v[138:141]
	v_mfma_f32_16x16x128_f8f6f4 v[134:137], v[2:9], v[58:65], v[134:137]
	s_setprio 0
	s_barrier
	v_lshl_add_u64 v[238:239], s[44:45], 0, v[214:215]
	s_add_i32 m0, s15, 0x18000
	ds_read_b128 v[58:61], v234 offset:49152
	ds_read_b128 v[62:65], v234 offset:50176
	ds_read_b128 v[50:53], v234 offset:51200
	ds_read_b128 v[54:57], v234 offset:52224
	ds_read_b128 v[42:45], v234 offset:53248
	ds_read_b128 v[46:49], v234 offset:54272
	ds_read_b128 v[34:37], v234 offset:55296
	ds_read_b128 v[38:41], v234 offset:56320
	global_load_lds_dwordx4 v[238:239], off
	s_add_i32 m0, s15, 0x1a000
	s_add_u32 s40, s40, 0x85000
	v_lshl_add_u64 v[238:239], s[44:45], 0, v[218:219]
	s_addc_u32 s41, s41, 0
	global_load_lds_dwordx4 v[238:239], off
	v_lshl_add_u64 v[238:239], s[40:41], 0, v[214:215]
	s_add_i32 m0, s15, 0x1c000
	v_lshl_add_u64 v[68:69], v[68:69], 0, s[8:9]
	global_load_lds_dwordx4 v[238:239], off
	v_lshl_add_u64 v[238:239], s[40:41], 0, v[218:219]
	s_add_i32 m0, s15, 0x1e000
	s_and_b64 vcc, exec, s[4:5]
	global_load_lds_dwordx4 v[238:239], off
	s_mov_b32 m0, s52
	s_nop 0
	global_load_lds_dwordx4 v[68:69], off
	v_lshl_add_u64 v[68:69], v[202:203], 0, s[8:9]
	s_mov_b32 m0, s53
	s_nop 0
	global_load_lds_dwordx4 v[68:69], off
	s_waitcnt vmcnt(8)
	s_waitcnt lgkmcnt(0)
	s_barrier
	s_cbranch_vccnz .LBB0_733
	s_setprio 1
	s_waitcnt lgkmcnt(0)
	v_mfma_f32_16x16x128_f8f6f4 v[130:133], v[26:33], v[58:65], v[130:133]
	v_mfma_f32_16x16x128_f8f6f4 v[126:129], v[18:25], v[58:65], v[126:129]
	v_mfma_f32_16x16x128_f8f6f4 v[114:117], v[26:33], v[50:57], v[114:117]
	v_mfma_f32_16x16x128_f8f6f4 v[110:113], v[18:25], v[50:57], v[110:113]
	v_mfma_f32_16x16x128_f8f6f4 v[98:101], v[26:33], v[42:49], v[98:101]
	v_mfma_f32_16x16x128_f8f6f4 v[94:97], v[18:25], v[42:49], v[94:97]
	v_mfma_f32_16x16x128_f8f6f4 v[82:85], v[26:33], v[34:41], v[82:85]
	v_mfma_f32_16x16x128_f8f6f4 v[78:81], v[18:25], v[34:41], v[78:81]
	s_setprio 0
	s_setprio 1
	v_mfma_f32_16x16x128_f8f6f4 v[122:125], v[10:17], v[58:65], v[122:125]
	v_mfma_f32_16x16x128_f8f6f4 v[118:121], v[2:9], v[58:65], v[118:121]
	v_mfma_f32_16x16x128_f8f6f4 v[106:109], v[10:17], v[50:57], v[106:109]
	v_mfma_f32_16x16x128_f8f6f4 v[102:105], v[2:9], v[50:57], v[102:105]
	v_mfma_f32_16x16x128_f8f6f4 v[90:93], v[10:17], v[42:49], v[90:93]
	v_mfma_f32_16x16x128_f8f6f4 v[86:89], v[2:9], v[42:49], v[86:89]
	v_mfma_f32_16x16x128_f8f6f4 v[74:77], v[10:17], v[34:41], v[74:77]
	v_mfma_f32_16x16x128_f8f6f4 v[70:73], v[2:9], v[34:41], v[70:73]
	s_setprio 0
	s_branch .LBB0_733

;     __device__ __forceinline__ void finish(v4i_t& t0, v4i_t& t1, int j, int tid) const {
;         asm volatile("" : "+v"(t0), "+v"(t1));
;         const float* s0; unsigned char* d; addr(j, tid, s0, d);
;         const f32x4 r0 = __builtin_bit_cast(f32x4, t0) * 64.f, r1 = __builtin_bit_cast(f32x4, t1) * 64.f;
;         int w0 = 0, w1 = 0; w0 = __builtin_amdgcn_cvt_pk_fp8_f32(r0[0], r1[0], w0, false); w0 = __builtin_amdgcn_cvt_pk_fp8_f32(r0[1], r1[1], w0, true);
;         w1 = __builtin_amdgcn_cvt_pk_fp8_f32(r0[2], r1[2], w1, false); w1 = __builtin_amdgcn_cvt_pk_fp8_f32(r0[3], r1[3], w1, true);
;         typedef int v2is __attribute__((ext_vector_type(2))); __builtin_nontemporal_store((v2is){w0, w1}, (v2is*)d);
.Lp7vg_wd_a1:
	s_waitcnt lgkmcnt(0)
	s_barrier
	s_cmp_lt_i32 s98, 0
	s_cbranch_scc1 .Lp7vg_mmslow_a
	s_cmpk_gt_i32 s48, 0x7f
	s_cbranch_scc1 .Lp7vg_mmslow_a
	s_setprio 1
	s_waitcnt lgkmcnt(0)
	v_mfma_f32_16x16x128_f8f6f4 v[202:205], v[26:33], v[58:65], v[202:205]
	s_add_i32 s4, s98, s52
	s_add_i32 s4, s4, 1
	v_pk_mul_f32 v[70:71], v[70:71], s[14:15] op_sel_hi:[1,0]
	v_pk_mul_f32 v[72:73], v[72:73], s[14:15] op_sel_hi:[1,0]
	v_mfma_f32_16x16x128_f8f6f4 v[198:201], v[18:25], v[58:65], v[198:201]
	v_pk_mul_f32 v[74:75], v[74:75], s[14:15] op_sel_hi:[1,0]
	v_pk_mul_f32 v[76:77], v[76:77], s[14:15] op_sel_hi:[1,0]
	s_ashr_i32 s2, s4, 10
	s_ashr_i32 s3, s2, 31
	v_mfma_f32_16x16x128_f8f6f4 v[186:189], v[26:33], v[50:57], v[186:189]
	v_cvt_pk_fp8_f32 v70, v70, v74
	s_lshl_b32 s4, s4, 12
	s_lshl_b64 s[2:3], s[2:3], 22
	v_cvt_pk_fp8_f32 v70, v71, v75 op_sel:[0,0,1]
	v_mfma_f32_16x16x128_f8f6f4 v[182:185], v[18:25], v[50:57], v[182:185]
	s_and_b32 s4, s4, 0x3ff000
	v_readlane_b32 s5, v251, 50
	v_cvt_pk_fp8_f32 v71, v72, v76
	s_add_u32 s2, s5, s2
	v_mfma_f32_16x16x128_f8f6f4 v[170:173], v[26:33], v[42:49], v[170:173]
	v_readlane_b32 s5, v251, 51
	s_addc_u32 s3, s5, s3
	v_cvt_pk_fp8_f32 v71, v73, v77 op_sel:[0,0,1]
	s_add_u32 s2, s2, s4
	s_addc_u32 s3, s3, 0
	v_mfma_f32_16x16x128_f8f6f4 v[166:169], v[18:25], v[42:49], v[166:169]
	v_lshl_add_u64 v[68:69], s[2:3], 0, v[210:211]
	global_store_dwordx2 v[68:69], v[70:71], off nt
	s_add_i32 s4, s48, s53
	s_ashr_i32 s2, s4, 10
	v_mfma_f32_16x16x128_f8f6f4 v[154:157], v[26:33], v[34:41], v[154:157]
	s_ashr_i32 s3, s2, 31
	s_lshl_b64 s[2:3], s[2:3], 24
	s_lshl_b32 s4, s4, 14
	s_and_b32 s4, s4, 0xffc000
	v_mfma_f32_16x16x128_f8f6f4 v[150:153], v[18:25], v[34:41], v[150:153]
	s_setprio 0
	s_setprio 1
	s_add_u32 s2, s76, s2
	s_addc_u32 s3, s77, s3
	s_add_u32 s2, s2, s4
	s_addc_u32 s3, s3, 0
	v_mfma_f32_16x16x128_f8f6f4 v[194:197], v[10:17], v[58:65], v[194:197]
	v_lshlrev_b32_e32 v66, 2, v208
	v_lshl_add_u64 v[68:69], s[2:3], 0, v[66:67]
	v_lshl_add_u64 v[68:69], v[68:69], 0, s[16:17]
	global_load_dwordx4 v[70:73], v66, s[2:3] nt
	v_mfma_f32_16x16x128_f8f6f4 v[190:193], v[2:9], v[58:65], v[190:193]
	global_load_dwordx4 v[74:77], v[68:69], off nt
	s_mov_b32 s100, 3
	s_mov_b32 s98, s48
	s_add_i32 s48, s48, 1
	v_mfma_f32_16x16x128_f8f6f4 v[178:181], v[10:17], v[50:57], v[178:181]
	s_add_u32 s2, s42, 0xfffc0080
	s_addc_u32 s3, s43, -1
	s_cmp_eq_u32 s64, 12
	s_cselect_b32 s5, s23, s3
	s_cselect_b32 s4, s25, s2
	s_cselect_b32 s45, s35, s63
	s_cselect_b32 s44, s61, s62
	v_mfma_f32_16x16x128_f8f6f4 v[174:177], v[2:9], v[50:57], v[174:177]
	v_mfma_f32_16x16x128_f8f6f4 v[162:165], v[10:17], v[42:49], v[162:165]
	v_mfma_f32_16x16x128_f8f6f4 v[158:161], v[2:9], v[42:49], v[158:161]
	v_mfma_f32_16x16x128_f8f6f4 v[146:149], v[10:17], v[34:41], v[146:149]
	v_mfma_f32_16x16x128_f8f6f4 v[142:145], v[2:9], v[34:41], v[142:145]
	s_setprio 0
	s_branch .Lp7vg_mmjoin_a

.Lp7vg_ni_a:
	s_add_u32 s2, s42, 0xfffc0080
	s_addc_u32 s3, s43, -1
	s_cmp_eq_u32 s64, 12
	s_cselect_b32 s5, s23, s3
	s_cselect_b32 s4, s25, s2
	s_cselect_b32 s45, s35, s63
	s_cselect_b32 s44, s61, s62
	s_setprio 1
	s_waitcnt lgkmcnt(0)
	v_mfma_f32_16x16x128_f8f6f4 v[202:205], v[26:33], v[58:65], v[202:205]
	v_mfma_f32_16x16x128_f8f6f4 v[198:201], v[18:25], v[58:65], v[198:201]
	v_mfma_f32_16x16x128_f8f6f4 v[186:189], v[26:33], v[50:57], v[186:189]
	v_mfma_f32_16x16x128_f8f6f4 v[182:185], v[18:25], v[50:57], v[182:185]
	v_mfma_f32_16x16x128_f8f6f4 v[170:173], v[26:33], v[42:49], v[170:173]
	v_mfma_f32_16x16x128_f8f6f4 v[166:169], v[18:25], v[42:49], v[166:169]
	v_mfma_f32_16x16x128_f8f6f4 v[154:157], v[26:33], v[34:41], v[154:157]
	v_mfma_f32_16x16x128_f8f6f4 v[150:153], v[18:25], v[34:41], v[150:153]
	s_setprio 0
	s_setprio 1
	v_mfma_f32_16x16x128_f8f6f4 v[194:197], v[10:17], v[58:65], v[194:197]
	v_mfma_f32_16x16x128_f8f6f4 v[190:193], v[2:9], v[58:65], v[190:193]
	v_mfma_f32_16x16x128_f8f6f4 v[178:181], v[10:17], v[50:57], v[178:181]
	v_mfma_f32_16x16x128_f8f6f4 v[174:177], v[2:9], v[50:57], v[174:177]
	v_mfma_f32_16x16x128_f8f6f4 v[162:165], v[10:17], v[42:49], v[162:165]
	v_mfma_f32_16x16x128_f8f6f4 v[158:161], v[2:9], v[42:49], v[158:161]
	v_mfma_f32_16x16x128_f8f6f4 v[146:149], v[10:17], v[34:41], v[146:149]
	v_mfma_f32_16x16x128_f8f6f4 v[142:145], v[2:9], v[34:41], v[142:145]
	s_setprio 0

.Lp7dma_wd_a:
	s_waitcnt lgkmcnt(0)
	s_barrier
	s_cbranch_vccnz .Lp7dma_skip_b
	s_setprio 1
	s_waitcnt lgkmcnt(0)
	v_mfma_f32_16x16x128_f8f6f4 v[138:141], v[26:33], v[58:65], v[138:141]
	v_mfma_f32_16x16x128_f8f6f4 v[134:137], v[18:25], v[58:65], v[134:137]
	v_mfma_f32_16x16x128_f8f6f4 v[122:125], v[26:33], v[50:57], v[122:125]
	v_mfma_f32_16x16x128_f8f6f4 v[118:121], v[18:25], v[50:57], v[118:121]
	v_mfma_f32_16x16x128_f8f6f4 v[106:109], v[26:33], v[42:49], v[106:109]
	v_mfma_f32_16x16x128_f8f6f4 v[102:105], v[18:25], v[42:49], v[102:105]
	v_mfma_f32_16x16x128_f8f6f4 v[90:93], v[26:33], v[34:41], v[90:93]
	v_mfma_f32_16x16x128_f8f6f4 v[86:89], v[18:25], v[34:41], v[86:89]
	s_setprio 0
	s_setprio 1
	v_mfma_f32_16x16x128_f8f6f4 v[130:133], v[10:17], v[58:65], v[130:133]
	v_mfma_f32_16x16x128_f8f6f4 v[126:129], v[2:9], v[58:65], v[126:129]
	v_mfma_f32_16x16x128_f8f6f4 v[114:117], v[10:17], v[50:57], v[114:117]
	v_lshl_add_u64 v[68:69], s[4:5], 0, v[212:213]
	s_mov_b32 m0, s15
	v_cmp_ne_u32_e64 s[2:3], 1, v66
	global_load_lds_dwordx4 v[68:69], off
	v_mfma_f32_16x16x128_f8f6f4 v[110:113], v[2:9], v[50:57], v[110:113]
	v_mfma_f32_16x16x128_f8f6f4 v[98:101], v[10:17], v[42:49], v[98:101]
	s_mov_b32 m0, s49
	s_nop 0
	global_load_lds_dwordx4 v[224:225], off
	v_mfma_f32_16x16x128_f8f6f4 v[94:97], v[2:9], v[42:49], v[94:97]
	v_mfma_f32_16x16x128_f8f6f4 v[82:85], v[10:17], v[34:41], v[82:85]
	v_mfma_f32_16x16x128_f8f6f4 v[78:81], v[2:9], v[34:41], v[78:81]
	s_setprio 0

;     __device__ __forceinline__ void finish(v4i_t& t0, v4i_t& t1, int j, int tid) const {
;         asm volatile("" : "+v"(t0), "+v"(t1));
;         const float* s0; unsigned char* d; addr(j, tid, s0, d);
;         const f32x4 r0 = __builtin_bit_cast(f32x4, t0) * 64.f, r1 = __builtin_bit_cast(f32x4, t1) * 64.f;
;         int w0 = 0, w1 = 0; w0 = __builtin_amdgcn_cvt_pk_fp8_f32(r0[0], r1[0], w0, false); w0 = __builtin_amdgcn_cvt_pk_fp8_f32(r0[1], r1[1], w0, true);
;         w1 = __builtin_amdgcn_cvt_pk_fp8_f32(r0[2], r1[2], w1, false); w1 = __builtin_amdgcn_cvt_pk_fp8_f32(r0[3], r1[3], w1, true);
;         typedef int v2is __attribute__((ext_vector_type(2))); __builtin_nontemporal_store((v2is){w0, w1}, (v2is*)d);
.Lp7vg_wd_b1:
	s_waitcnt lgkmcnt(0)
	s_barrier
	s_cmp_lt_i32 s99, 0
	s_cbranch_scc1 .Lp7vg_mmslow_b
	s_cmpk_gt_i32 s48, 0x7f
	s_cbranch_scc1 .Lp7vg_mmslow_b
	s_setprio 1
	s_waitcnt lgkmcnt(0)
	v_mfma_f32_16x16x128_f8f6f4 v[202:205], v[26:33], v[58:65], v[202:205]
	s_add_i32 s65, s99, s52
	s_add_i32 s65, s65, 1
	v_pk_mul_f32 v[242:243], v[242:243], s[14:15] op_sel_hi:[1,0]
	v_pk_mul_f32 v[244:245], v[244:245], s[14:15] op_sel_hi:[1,0]
	v_mfma_f32_16x16x128_f8f6f4 v[198:201], v[18:25], v[58:65], v[198:201]
	v_pk_mul_f32 v[246:247], v[246:247], s[14:15] op_sel_hi:[1,0]
	v_pk_mul_f32 v[248:249], v[248:249], s[14:15] op_sel_hi:[1,0]
	s_ashr_i32 s46, s65, 10
	s_ashr_i32 s47, s46, 31
	v_mfma_f32_16x16x128_f8f6f4 v[186:189], v[26:33], v[50:57], v[186:189]
	v_cvt_pk_fp8_f32 v242, v242, v246
	s_lshl_b32 s65, s65, 12
	s_lshl_b64 s[46:47], s[46:47], 22
	v_cvt_pk_fp8_f32 v242, v243, v247 op_sel:[0,0,1]
	v_mfma_f32_16x16x128_f8f6f4 v[182:185], v[18:25], v[50:57], v[182:185]
	s_and_b32 s65, s65, 0x3ff000
	v_readlane_b32 s4, v251, 50
	v_cvt_pk_fp8_f32 v243, v244, v248
	s_add_u32 s46, s4, s46
	v_mfma_f32_16x16x128_f8f6f4 v[170:173], v[26:33], v[42:49], v[170:173]
	v_readlane_b32 s4, v251, 51
	s_addc_u32 s47, s4, s47
	v_cvt_pk_fp8_f32 v243, v245, v249 op_sel:[0,0,1]
	s_add_u32 s46, s46, s65
	s_addc_u32 s47, s47, 0
	v_mfma_f32_16x16x128_f8f6f4 v[166:169], v[18:25], v[42:49], v[166:169]
	v_lshl_add_u64 v[240:241], s[46:47], 0, v[210:211]
	global_store_dwordx2 v[240:241], v[242:243], off nt
	s_add_i32 s65, s48, s53
	s_ashr_i32 s46, s65, 10
	v_mfma_f32_16x16x128_f8f6f4 v[154:157], v[26:33], v[34:41], v[154:157]
	s_ashr_i32 s47, s46, 31
	s_lshl_b64 s[46:47], s[46:47], 24
	s_lshl_b32 s65, s65, 14
	s_and_b32 s65, s65, 0xffc000
	v_mfma_f32_16x16x128_f8f6f4 v[150:153], v[18:25], v[34:41], v[150:153]
	s_setprio 0
	s_setprio 1
	s_add_u32 s46, s76, s46
	s_addc_u32 s47, s77, s47
	s_add_u32 s46, s46, s65
	s_addc_u32 s47, s47, 0
	v_mfma_f32_16x16x128_f8f6f4 v[194:197], v[10:17], v[58:65], v[194:197]
	v_lshlrev_b32_e32 v66, 2, v208
	v_lshl_add_u64 v[240:241], s[46:47], 0, v[66:67]
	v_lshl_add_u64 v[240:241], v[240:241], 0, s[16:17]
	global_load_dwordx4 v[242:245], v66, s[46:47] nt
	v_mfma_f32_16x16x128_f8f6f4 v[190:193], v[2:9], v[58:65], v[190:193]
	global_load_dwordx4 v[246:249], v[240:241], off nt
	s_mov_b32 s100, 3
	s_mov_b32 s99, s48
	s_add_i32 s48, s48, 1
	v_mfma_f32_16x16x128_f8f6f4 v[178:181], v[10:17], v[50:57], v[178:181]
	s_add_u32 s46, s44, 0x84000
	s_addc_u32 s47, s45, 0
	v_mfma_f32_16x16x128_f8f6f4 v[174:177], v[2:9], v[50:57], v[174:177]
	v_mfma_f32_16x16x128_f8f6f4 v[162:165], v[10:17], v[42:49], v[162:165]
	v_mfma_f32_16x16x128_f8f6f4 v[158:161], v[2:9], v[42:49], v[158:161]
	v_mfma_f32_16x16x128_f8f6f4 v[146:149], v[10:17], v[34:41], v[146:149]
	v_mfma_f32_16x16x128_f8f6f4 v[142:145], v[2:9], v[34:41], v[142:145]
	s_setprio 0
	s_branch .Lp7vg_mmjoin_b

.Lp7vg_ni_b:
	s_add_u32 s46, s44, 0x84000
	s_addc_u32 s47, s45, 0
	s_setprio 1
	s_waitcnt lgkmcnt(0)
	v_mfma_f32_16x16x128_f8f6f4 v[202:205], v[26:33], v[58:65], v[202:205]
	v_mfma_f32_16x16x128_f8f6f4 v[198:201], v[18:25], v[58:65], v[198:201]
	v_mfma_f32_16x16x128_f8f6f4 v[186:189], v[26:33], v[50:57], v[186:189]
	v_mfma_f32_16x16x128_f8f6f4 v[182:185], v[18:25], v[50:57], v[182:185]
	v_mfma_f32_16x16x128_f8f6f4 v[170:173], v[26:33], v[42:49], v[170:173]
	v_mfma_f32_16x16x128_f8f6f4 v[166:169], v[18:25], v[42:49], v[166:169]
	v_mfma_f32_16x16x128_f8f6f4 v[154:157], v[26:33], v[34:41], v[154:157]
	v_mfma_f32_16x16x128_f8f6f4 v[150:153], v[18:25], v[34:41], v[150:153]
	s_setprio 0
	s_setprio 1
	v_mfma_f32_16x16x128_f8f6f4 v[194:197], v[10:17], v[58:65], v[194:197]
	v_mfma_f32_16x16x128_f8f6f4 v[190:193], v[2:9], v[58:65], v[190:193]
	v_mfma_f32_16x16x128_f8f6f4 v[178:181], v[10:17], v[50:57], v[178:181]
	v_mfma_f32_16x16x128_f8f6f4 v[174:177], v[2:9], v[50:57], v[174:177]
	v_mfma_f32_16x16x128_f8f6f4 v[162:165], v[10:17], v[42:49], v[162:165]
	v_mfma_f32_16x16x128_f8f6f4 v[158:161], v[2:9], v[42:49], v[158:161]
	v_mfma_f32_16x16x128_f8f6f4 v[146:149], v[10:17], v[34:41], v[146:149]
	v_mfma_f32_16x16x128_f8f6f4 v[142:145], v[2:9], v[34:41], v[142:145]
	s_setprio 0

.Lp7dma_wd_b:
	s_waitcnt lgkmcnt(0)
	s_barrier
	s_cbranch_vccnz .Lp7dma_skip_d
	s_setprio 1
	s_waitcnt lgkmcnt(0)
	v_mfma_f32_16x16x128_f8f6f4 v[138:141], v[26:33], v[58:65], v[138:141]
	v_mfma_f32_16x16x128_f8f6f4 v[134:137], v[18:25], v[58:65], v[134:137]
	v_mfma_f32_16x16x128_f8f6f4 v[122:125], v[26:33], v[50:57], v[122:125]
	v_mfma_f32_16x16x128_f8f6f4 v[118:121], v[18:25], v[50:57], v[118:121]
	v_mfma_f32_16x16x128_f8f6f4 v[106:109], v[26:33], v[42:49], v[106:109]
	v_mfma_f32_16x16x128_f8f6f4 v[102:105], v[18:25], v[42:49], v[102:105]
	v_mfma_f32_16x16x128_f8f6f4 v[90:93], v[26:33], v[34:41], v[90:93]
	v_mfma_f32_16x16x128_f8f6f4 v[86:89], v[18:25], v[34:41], v[86:89]
	s_setprio 0
	s_setprio 1
	v_mfma_f32_16x16x128_f8f6f4 v[130:133], v[10:17], v[58:65], v[130:133]
	v_mfma_f32_16x16x128_f8f6f4 v[126:129], v[2:9], v[58:65], v[126:129]
	v_mfma_f32_16x16x128_f8f6f4 v[114:117], v[10:17], v[50:57], v[114:117]
	s_mov_b32 m0, s54
	s_nop 0
	global_load_lds_dwordx4 v[68:69], off
	v_mfma_f32_16x16x128_f8f6f4 v[110:113], v[2:9], v[50:57], v[110:113]
	v_mfma_f32_16x16x128_f8f6f4 v[98:101], v[10:17], v[42:49], v[98:101]
	v_lshl_add_u64 v[68:69], v[224:225], 0, s[10:11]
	s_mov_b32 m0, s55
	s_nop 0
	global_load_lds_dwordx4 v[68:69], off
	v_mfma_f32_16x16x128_f8f6f4 v[94:97], v[2:9], v[42:49], v[94:97]
	v_mfma_f32_16x16x128_f8f6f4 v[82:85], v[10:17], v[34:41], v[82:85]
	v_mfma_f32_16x16x128_f8f6f4 v[78:81], v[2:9], v[34:41], v[78:81]
	s_setprio 0
	s_branch .LBB0_781

.LBB0_901:
	ds_read_b64_tr_b16 v[26:27], v207 offset:0
	ds_read_b64_tr_b16 v[28:29], v207 offset:1024
	ds_read_b64_tr_b16 v[30:31], v207 offset:8192
	ds_read_b64_tr_b16 v[32:33], v207 offset:9216
	ds_read_b64_tr_b16 v[18:19], v217 offset:0
	ds_read_b64_tr_b16 v[20:21], v217 offset:1024
	ds_read_b64_tr_b16 v[22:23], v217 offset:8192
	ds_read_b64_tr_b16 v[24:25], v217 offset:9216
	ds_read_b64_tr_b16 v[10:11], v214 offset:0
	ds_read_b64_tr_b16 v[12:13], v214 offset:1024
	ds_read_b64_tr_b16 v[14:15], v214 offset:8192
	ds_read_b64_tr_b16 v[16:17], v214 offset:9216
	ds_read_b64_tr_b16 v[2:3], v218 offset:0
	ds_read_b64_tr_b16 v[4:5], v218 offset:1024
	ds_read_b64_tr_b16 v[6:7], v218 offset:8192
	ds_read_b64_tr_b16 v[8:9], v218 offset:9216
	s_add_u32 s2, s50, 0xfffc0080
	s_addc_u32 s3, s51, -1
	s_cmp_eq_u32 s72, 12
	s_cselect_b32 s55, s29, s3
	s_cselect_b32 s54, s31, s2
	s_cselect_b32 s53, s35, s71
	s_cselect_b32 s52, s43, s70
	ds_read_b128 v[34:37], v223
	ds_read_b128 v[38:41], v223 offset:1024
	ds_read_b128 v[42:45], v223 offset:2048
	ds_read_b128 v[46:49], v223 offset:3072
	ds_read_b128 v[50:53], v223 offset:4096
	ds_read_b128 v[54:57], v223 offset:5120
	ds_read_b128 v[58:61], v223 offset:6144
	ds_read_b128 v[62:65], v223 offset:7168
	s_waitcnt vmcnt(6)
	s_waitcnt lgkmcnt(0)
	s_barrier
	s_setprio 1
	s_waitcnt lgkmcnt(0)
	v_mfma_f32_16x16x128_f8f6f4 v[194:197], v[26:33], v[34:41], v[194:197]
	v_mfma_f32_16x16x128_f8f6f4 v[190:193], v[18:25], v[34:41], v[190:193]
	v_mfma_f32_16x16x128_f8f6f4 v[186:189], v[26:33], v[42:49], v[186:189]
	v_mfma_f32_16x16x128_f8f6f4 v[182:185], v[18:25], v[42:49], v[182:185]
	v_lshl_add_u64 v[68:69], s[50:51], 0, v[208:209]
	s_add_i32 m0, s17, 0xc000
	s_nop 0
	global_load_lds_dwordx4 v[68:69], off
	v_mfma_f32_16x16x128_f8f6f4 v[162:165], v[26:33], v[50:57], v[162:165]
	v_mfma_f32_16x16x128_f8f6f4 v[158:161], v[18:25], v[50:57], v[158:161]
	v_mfma_f32_16x16x128_f8f6f4 v[146:149], v[26:33], v[58:65], v[146:149]
	v_mfma_f32_16x16x128_f8f6f4 v[142:145], v[18:25], v[58:65], v[142:145]
	s_setprio 0
	s_setprio 1
	v_mfma_f32_16x16x128_f8f6f4 v[178:181], v[10:17], v[34:41], v[178:181]
	v_mfma_f32_16x16x128_f8f6f4 v[174:177], v[2:9], v[34:41], v[174:177]
	v_lshl_add_u64 v[68:69], s[50:51], 0, v[210:211]
	s_add_i32 m0, s17, 0xe000
	s_nop 0
	global_load_lds_dwordx4 v[68:69], off
	v_mfma_f32_16x16x128_f8f6f4 v[170:173], v[10:17], v[42:49], v[170:173]
	v_mfma_f32_16x16x128_f8f6f4 v[166:169], v[2:9], v[42:49], v[166:169]
	v_mfma_f32_16x16x128_f8f6f4 v[154:157], v[10:17], v[50:57], v[154:157]
	v_mfma_f32_16x16x128_f8f6f4 v[150:153], v[2:9], v[50:57], v[150:153]
	v_mfma_f32_16x16x128_f8f6f4 v[138:141], v[10:17], v[58:65], v[138:141]
	v_mfma_f32_16x16x128_f8f6f4 v[134:137], v[2:9], v[58:65], v[134:137]
	s_setprio 0
	s_barrier
	s_mov_b32 m0, s19
	v_lshl_add_u64 v[68:69], s[52:53], 0, v[200:201]
	global_load_lds_dwordx4 v[68:69], off
	v_lshl_add_u64 v[212:213], s[52:53], 0, v[204:205]
	s_mov_b32 m0, s33
	v_lshl_add_u64 v[68:69], v[68:69], 0, s[4:5]
	global_load_lds_dwordx4 v[212:213], off
	s_mov_b32 m0, s45
	s_nop 0
	global_load_lds_dwordx4 v[68:69], off
	v_lshl_add_u64 v[68:69], v[212:213], 0, s[4:5]
	s_mov_b32 m0, s47
	v_lshl_add_u64 v[212:213], s[54:55], 0, v[202:203]
	global_load_lds_dwordx4 v[68:69], off
	s_andn2_b64 vcc, exec, s[48:49]
	s_cbranch_vccnz .Lhalfskip_p8a
	ds_read_b128 v[58:61], v223 offset:16384
	ds_read_b128 v[62:65], v223 offset:17408
	ds_read_b128 v[50:53], v223 offset:18432
	ds_read_b128 v[54:57], v223 offset:19456
	ds_read_b128 v[42:45], v223 offset:20480
	ds_read_b128 v[46:49], v223 offset:21504
	ds_read_b128 v[34:37], v223 offset:22528
	ds_read_b128 v[38:41], v223 offset:23552
.Lhalfskip_p8a:
	v_cmp_ne_u32_e64 s[2:3], 1, v225
	s_waitcnt vmcnt(6)
	s_waitcnt lgkmcnt(0)
	s_barrier
	s_cbranch_vccnz .Lp8_skip_b
	s_setprio 1
	s_waitcnt lgkmcnt(0)
	v_mfma_f32_16x16x128_f8f6f4 v[130:133], v[26:33], v[58:65], v[130:133]
	v_mfma_f32_16x16x128_f8f6f4 v[126:129], v[18:25], v[58:65], v[126:129]
	v_mfma_f32_16x16x128_f8f6f4 v[114:117], v[26:33], v[50:57], v[114:117]
	v_mfma_f32_16x16x128_f8f6f4 v[110:113], v[18:25], v[50:57], v[110:113]
	v_mfma_f32_16x16x128_f8f6f4 v[98:101], v[26:33], v[42:49], v[98:101]
	v_mfma_f32_16x16x128_f8f6f4 v[94:97], v[18:25], v[42:49], v[94:97]
	v_mfma_f32_16x16x128_f8f6f4 v[82:85], v[26:33], v[34:41], v[82:85]
	v_mfma_f32_16x16x128_f8f6f4 v[78:81], v[18:25], v[34:41], v[78:81]
	s_setprio 0
	s_setprio 1
	v_mfma_f32_16x16x128_f8f6f4 v[122:125], v[10:17], v[58:65], v[122:125]
	v_mfma_f32_16x16x128_f8f6f4 v[118:121], v[2:9], v[58:65], v[118:121]
	v_mfma_f32_16x16x128_f8f6f4 v[106:109], v[10:17], v[50:57], v[106:109]
	v_lshl_add_u64 v[68:69], s[54:55], 0, v[198:199]
	s_mov_b32 m0, s17
	s_nop 0
	global_load_lds_dwordx4 v[68:69], off
	v_mfma_f32_16x16x128_f8f6f4 v[102:105], v[2:9], v[50:57], v[102:105]
	v_mfma_f32_16x16x128_f8f6f4 v[90:93], v[10:17], v[42:49], v[90:93]
	s_mov_b32 m0, s58
	s_nop 0
	global_load_lds_dwordx4 v[212:213], off
	v_mfma_f32_16x16x128_f8f6f4 v[86:89], v[2:9], v[42:49], v[86:89]
	v_mfma_f32_16x16x128_f8f6f4 v[74:77], v[10:17], v[34:41], v[74:77]
	v_mfma_f32_16x16x128_f8f6f4 v[70:73], v[2:9], v[34:41], v[70:73]
	s_setprio 0
.LBB0_903:
	s_add_u32 s56, s52, 0x40000
	s_addc_u32 s57, s53, 0
	s_barrier
	ds_read_b64_tr_b16 v[26:27], v215 offset:0
	ds_read_b64_tr_b16 v[28:29], v215 offset:1024
	ds_read_b64_tr_b16 v[30:31], v215 offset:8192
	ds_read_b64_tr_b16 v[32:33], v215 offset:9216
	ds_read_b64_tr_b16 v[18:19], v219 offset:0
	ds_read_b64_tr_b16 v[20:21], v219 offset:1024
	ds_read_b64_tr_b16 v[22:23], v219 offset:8192
	ds_read_b64_tr_b16 v[24:25], v219 offset:9216
	ds_read_b64_tr_b16 v[10:11], v216 offset:0
	ds_read_b64_tr_b16 v[12:13], v216 offset:1024
	ds_read_b64_tr_b16 v[14:15], v216 offset:8192
	ds_read_b64_tr_b16 v[16:17], v216 offset:9216
	ds_read_b64_tr_b16 v[2:3], v220 offset:0
	ds_read_b64_tr_b16 v[4:5], v220 offset:1024
	ds_read_b64_tr_b16 v[6:7], v220 offset:8192
	ds_read_b64_tr_b16 v[8:9], v220 offset:9216
	s_add_u32 s54, s54, 0x40000
	s_addc_u32 s55, s55, 0
	ds_read_b128 v[34:37], v223 offset:32768
	ds_read_b128 v[38:41], v223 offset:33792
	ds_read_b128 v[42:45], v223 offset:34816
	ds_read_b128 v[46:49], v223 offset:35840
	ds_read_b128 v[50:53], v223 offset:36864
	ds_read_b128 v[54:57], v223 offset:37888
	ds_read_b128 v[58:61], v223 offset:38912
	ds_read_b128 v[62:65], v223 offset:39936
	s_waitcnt vmcnt(6)
	s_waitcnt lgkmcnt(0)
	s_barrier
	s_setprio 1
	s_waitcnt lgkmcnt(0)
	v_mfma_f32_16x16x128_f8f6f4 v[194:197], v[26:33], v[34:41], v[194:197]
	v_mfma_f32_16x16x128_f8f6f4 v[190:193], v[18:25], v[34:41], v[190:193]
	v_mfma_f32_16x16x128_f8f6f4 v[186:189], v[26:33], v[42:49], v[186:189]
	v_mfma_f32_16x16x128_f8f6f4 v[182:185], v[18:25], v[42:49], v[182:185]
	s_mov_b32 m0, s59
	v_lshl_add_u64 v[226:227], s[54:55], 0, v[198:199]
	global_load_lds_dwordx4 v[226:227], off
	v_mfma_f32_16x16x128_f8f6f4 v[162:165], v[26:33], v[50:57], v[162:165]
	v_mfma_f32_16x16x128_f8f6f4 v[158:161], v[18:25], v[50:57], v[158:161]
	v_mfma_f32_16x16x128_f8f6f4 v[146:149], v[26:33], v[58:65], v[146:149]
	v_mfma_f32_16x16x128_f8f6f4 v[142:145], v[18:25], v[58:65], v[142:145]
	s_setprio 0
	s_setprio 1
	v_mfma_f32_16x16x128_f8f6f4 v[178:181], v[10:17], v[34:41], v[178:181]
	v_mfma_f32_16x16x128_f8f6f4 v[174:177], v[2:9], v[34:41], v[174:177]
	v_lshl_add_u64 v[226:227], s[54:55], 0, v[202:203]
	s_mov_b32 m0, s60
	s_nop 0
	global_load_lds_dwordx4 v[226:227], off
	v_mfma_f32_16x16x128_f8f6f4 v[170:173], v[10:17], v[42:49], v[170:173]
	v_mfma_f32_16x16x128_f8f6f4 v[166:169], v[2:9], v[42:49], v[166:169]
	v_mfma_f32_16x16x128_f8f6f4 v[154:157], v[10:17], v[50:57], v[154:157]
	v_mfma_f32_16x16x128_f8f6f4 v[150:153], v[2:9], v[50:57], v[150:153]
	v_mfma_f32_16x16x128_f8f6f4 v[138:141], v[10:17], v[58:65], v[138:141]
	v_mfma_f32_16x16x128_f8f6f4 v[134:137], v[2:9], v[58:65], v[134:137]
	s_setprio 0
	s_barrier
	v_lshl_add_u64 v[226:227], s[56:57], 0, v[200:201]
	s_add_i32 m0, s17, 0x18000
	s_nop 0
	global_load_lds_dwordx4 v[226:227], off
	s_add_i32 m0, s17, 0x1a000
	v_lshl_add_u64 v[226:227], s[56:57], 0, v[204:205]
	global_load_lds_dwordx4 v[226:227], off
	s_add_u32 s52, s52, 0x40100
	s_addc_u32 s53, s53, 0
	v_lshl_add_u64 v[226:227], s[52:53], 0, v[200:201]
	s_add_i32 m0, s17, 0x1c000
	v_lshl_add_u64 v[68:69], v[68:69], 0, s[12:13]
	global_load_lds_dwordx4 v[226:227], off
	v_lshl_add_u64 v[226:227], s[52:53], 0, v[204:205]
	s_add_i32 m0, s17, 0x1e000
	s_nop 0
	global_load_lds_dwordx4 v[226:227], off
	s_and_b64 vcc, exec, s[2:3]
	s_cbranch_vccnz .Lhalfskip_p8b
	ds_read_b128 v[58:61], v223 offset:49152
	ds_read_b128 v[62:65], v223 offset:50176
	ds_read_b128 v[50:53], v223 offset:51200
	ds_read_b128 v[54:57], v223 offset:52224
	ds_read_b128 v[42:45], v223 offset:53248
	ds_read_b128 v[46:49], v223 offset:54272
	ds_read_b128 v[34:37], v223 offset:55296
	ds_read_b128 v[38:41], v223 offset:56320
.Lhalfskip_p8b:
	s_waitcnt vmcnt(6)
	s_waitcnt lgkmcnt(0)
	s_barrier
	s_cbranch_vccnz .Lp8_skip_d
	s_setprio 1
	s_waitcnt lgkmcnt(0)
	v_mfma_f32_16x16x128_f8f6f4 v[130:133], v[26:33], v[58:65], v[130:133]
	v_mfma_f32_16x16x128_f8f6f4 v[126:129], v[18:25], v[58:65], v[126:129]
	v_mfma_f32_16x16x128_f8f6f4 v[114:117], v[26:33], v[50:57], v[114:117]
	v_mfma_f32_16x16x128_f8f6f4 v[110:113], v[18:25], v[50:57], v[110:113]
	v_mfma_f32_16x16x128_f8f6f4 v[98:101], v[26:33], v[42:49], v[98:101]
	v_mfma_f32_16x16x128_f8f6f4 v[94:97], v[18:25], v[42:49], v[94:97]
	v_mfma_f32_16x16x128_f8f6f4 v[82:85], v[26:33], v[34:41], v[82:85]
	v_mfma_f32_16x16x128_f8f6f4 v[78:81], v[18:25], v[34:41], v[78:81]
	s_setprio 0
	s_setprio 1
	v_mfma_f32_16x16x128_f8f6f4 v[122:125], v[10:17], v[58:65], v[122:125]
	v_mfma_f32_16x16x128_f8f6f4 v[118:121], v[2:9], v[58:65], v[118:121]
	v_mfma_f32_16x16x128_f8f6f4 v[106:109], v[10:17], v[50:57], v[106:109]
	s_mov_b32 m0, s62
	s_nop 0
	global_load_lds_dwordx4 v[68:69], off
	v_mfma_f32_16x16x128_f8f6f4 v[102:105], v[2:9], v[50:57], v[102:105]
	v_mfma_f32_16x16x128_f8f6f4 v[90:93], v[10:17], v[42:49], v[90:93]
	v_lshl_add_u64 v[68:69], v[212:213], 0, s[12:13]
	s_mov_b32 m0, s63
	s_nop 0
	global_load_lds_dwordx4 v[68:69], off
	v_mfma_f32_16x16x128_f8f6f4 v[86:89], v[2:9], v[42:49], v[86:89]
	v_mfma_f32_16x16x128_f8f6f4 v[74:77], v[10:17], v[34:41], v[74:77]
	v_mfma_f32_16x16x128_f8f6f4 v[70:73], v[2:9], v[34:41], v[70:73]
	s_setprio 0
	s_branch .LBB0_900
